# stageA: W1 conversion loop de-serialized (32 loads in flight instead of 4+wait x16); sort sweeps: 28 streaming loads issued back-to-back (no per-sweep vmcnt(0)/copy)
# speedup vs baseline: 1.0187x; 1.0129x over previous
.LBB1_4:
	s_or_b64 exec, exec, s[4:5]
	s_load_dwordx2 s[14:15], s[0:1], 0x68
	s_load_dwordx4 s[4:7], s[0:1], 0x58
	v_and_b32_e32 v3, 0x7f, v0
	v_lshlrev_b32_e32 v4, 2, v3
	v_mov_b32_e32 v5, 0
	v_and_b32_e32 v11, 63, v0
	s_waitcnt lgkmcnt(0)
	v_lshl_add_u64 v[6:7], s[12:13], 0, v[4:5]
	v_mul_u32_u24_e32 v3, 0x110, v3
	v_or_b32_e32 v12, 0xffffff00, v0
	v_lshrrev_b32_e32 v13, 5, v0
	s_mov_b64 s[18:19], 0
	s_movk_i32 s3, 0xeff
	v_and_b32_e32 v16, 0x7c, v13
	v_lshlrev_b32_e32 v4, 9, v16
	v_and_b32_e32 v14, 0x7f, v0
	v_lshl_add_u32 v14, v14, 2, v4
	v_lshl_add_u32 v16, v16, 1, v3
	global_load_dword v66, v14, s[12:13]
	global_load_dword v67, v14, s[12:13] offset:512
	global_load_dword v68, v14, s[12:13] offset:1024
	global_load_dword v69, v14, s[12:13] offset:1536
	v_add_u32_e32 v14, 0x1000, v14
	global_load_dword v70, v14, s[12:13]
	global_load_dword v71, v14, s[12:13] offset:512
	global_load_dword v72, v14, s[12:13] offset:1024
	global_load_dword v73, v14, s[12:13] offset:1536
	v_add_u32_e32 v14, 0x1000, v14
	global_load_dword v74, v14, s[12:13]
	global_load_dword v75, v14, s[12:13] offset:512
	global_load_dword v76, v14, s[12:13] offset:1024
	global_load_dword v77, v14, s[12:13] offset:1536
	v_add_u32_e32 v14, 0x1000, v14
	global_load_dword v78, v14, s[12:13]
	global_load_dword v79, v14, s[12:13] offset:512
	global_load_dword v80, v14, s[12:13] offset:1024
	global_load_dword v81, v14, s[12:13] offset:1536
	v_add_u32_e32 v14, 0x1000, v14
	global_load_dword v82, v14, s[12:13]
	global_load_dword v83, v14, s[12:13] offset:512
	global_load_dword v84, v14, s[12:13] offset:1024
	global_load_dword v85, v14, s[12:13] offset:1536
	v_add_u32_e32 v14, 0x1000, v14
	global_load_dword v86, v14, s[12:13]
	global_load_dword v87, v14, s[12:13] offset:512
	global_load_dword v88, v14, s[12:13] offset:1024
	global_load_dword v89, v14, s[12:13] offset:1536
	v_add_u32_e32 v14, 0x1000, v14
	global_load_dword v90, v14, s[12:13]
	global_load_dword v91, v14, s[12:13] offset:512
	global_load_dword v92, v14, s[12:13] offset:1024
	global_load_dword v93, v14, s[12:13] offset:1536
	v_add_u32_e32 v14, 0x1000, v14
	global_load_dword v94, v14, s[12:13]
	global_load_dword v95, v14, s[12:13] offset:512
	global_load_dword v96, v14, s[12:13] offset:1024
	global_load_dword v97, v14, s[12:13] offset:1536
	v_add_u32_e32 v14, 0x1000, v14
	s_waitcnt vmcnt(28)
	v_cvt_pk_f16_f32 v66, v66, v67
	v_cvt_pk_f16_f32 v67, v68, v69
	ds_write_b64 v16, v[66:67]
	global_load_dword v98, v14, s[12:13]
	global_load_dword v99, v14, s[12:13] offset:512
	global_load_dword v100, v14, s[12:13] offset:1024
	global_load_dword v101, v14, s[12:13] offset:1536
	v_add_u32_e32 v14, 0x1000, v14
	s_waitcnt vmcnt(28)
	v_cvt_pk_f16_f32 v70, v70, v71
	v_cvt_pk_f16_f32 v71, v72, v73
	ds_write_b64 v16, v[70:71] offset:16
	global_load_dword v102, v14, s[12:13]
	global_load_dword v103, v14, s[12:13] offset:512
	global_load_dword v104, v14, s[12:13] offset:1024
	global_load_dword v105, v14, s[12:13] offset:1536
	v_add_u32_e32 v14, 0x1000, v14
	s_waitcnt vmcnt(28)
	v_cvt_pk_f16_f32 v74, v74, v75
	v_cvt_pk_f16_f32 v75, v76, v77
	ds_write_b64 v16, v[74:75] offset:32
	global_load_dword v106, v14, s[12:13]
	global_load_dword v107, v14, s[12:13] offset:512
	global_load_dword v108, v14, s[12:13] offset:1024
	global_load_dword v109, v14, s[12:13] offset:1536
	v_add_u32_e32 v14, 0x1000, v14
	s_waitcnt vmcnt(28)
	v_cvt_pk_f16_f32 v78, v78, v79
	v_cvt_pk_f16_f32 v79, v80, v81
	ds_write_b64 v16, v[78:79] offset:48
	global_load_dword v110, v14, s[12:13]
	global_load_dword v111, v14, s[12:13] offset:512
	global_load_dword v112, v14, s[12:13] offset:1024
	global_load_dword v113, v14, s[12:13] offset:1536
	v_add_u32_e32 v14, 0x1000, v14
	s_waitcnt vmcnt(28)
	v_cvt_pk_f16_f32 v82, v82, v83
	v_cvt_pk_f16_f32 v83, v84, v85
	ds_write_b64 v16, v[82:83] offset:64
	global_load_dword v114, v14, s[12:13]
	global_load_dword v115, v14, s[12:13] offset:512
	global_load_dword v116, v14, s[12:13] offset:1024
	global_load_dword v117, v14, s[12:13] offset:1536
	v_add_u32_e32 v14, 0x1000, v14
	s_waitcnt vmcnt(28)
	v_cvt_pk_f16_f32 v86, v86, v87
	v_cvt_pk_f16_f32 v87, v88, v89
	ds_write_b64 v16, v[86:87] offset:80
	global_load_dword v118, v14, s[12:13]
	global_load_dword v119, v14, s[12:13] offset:512
	global_load_dword v120, v14, s[12:13] offset:1024
	global_load_dword v121, v14, s[12:13] offset:1536
	v_add_u32_e32 v14, 0x1000, v14
	s_waitcnt vmcnt(28)
	v_cvt_pk_f16_f32 v90, v90, v91
	v_cvt_pk_f16_f32 v91, v92, v93
	ds_write_b64 v16, v[90:91] offset:96
	global_load_dword v122, v14, s[12:13]
	global_load_dword v123, v14, s[12:13] offset:512
	global_load_dword v124, v14, s[12:13] offset:1024
	global_load_dword v125, v14, s[12:13] offset:1536
	v_add_u32_e32 v14, 0x1000, v14
	s_waitcnt vmcnt(28)
	v_cvt_pk_f16_f32 v94, v94, v95
	v_cvt_pk_f16_f32 v95, v96, v97
	ds_write_b64 v16, v[94:95] offset:112
	global_load_dword v126, v14, s[12:13]
	global_load_dword v127, v14, s[12:13] offset:512
	global_load_dword v128, v14, s[12:13] offset:1024
	global_load_dword v129, v14, s[12:13] offset:1536
	s_waitcnt vmcnt(28)
	v_cvt_pk_f16_f32 v98, v98, v99
	v_cvt_pk_f16_f32 v99, v100, v101
	ds_write_b64 v16, v[98:99] offset:128
	s_waitcnt vmcnt(24)
	v_cvt_pk_f16_f32 v102, v102, v103
	v_cvt_pk_f16_f32 v103, v104, v105
	ds_write_b64 v16, v[102:103] offset:144
	s_waitcnt vmcnt(20)
	v_cvt_pk_f16_f32 v106, v106, v107
	v_cvt_pk_f16_f32 v107, v108, v109
	ds_write_b64 v16, v[106:107] offset:160
	s_waitcnt vmcnt(16)
	v_cvt_pk_f16_f32 v110, v110, v111
	v_cvt_pk_f16_f32 v111, v112, v113
	ds_write_b64 v16, v[110:111] offset:176
	s_waitcnt vmcnt(12)
	v_cvt_pk_f16_f32 v114, v114, v115
	v_cvt_pk_f16_f32 v115, v116, v117
	ds_write_b64 v16, v[114:115] offset:192
	s_waitcnt vmcnt(8)
	v_cvt_pk_f16_f32 v118, v118, v119
	v_cvt_pk_f16_f32 v119, v120, v121
	ds_write_b64 v16, v[118:119] offset:208
	s_waitcnt vmcnt(4)
	v_cvt_pk_f16_f32 v122, v122, v123
	v_cvt_pk_f16_f32 v123, v124, v125
	ds_write_b64 v16, v[122:123] offset:224
	s_waitcnt vmcnt(0)
	v_cvt_pk_f16_f32 v126, v126, v127
	v_cvt_pk_f16_f32 v127, v128, v129
	ds_write_b64 v16, v[126:127] offset:240
	s_movk_i32 s3, 0x80
	v_cmp_gt_u32_e32 vcc, s3, v0
	s_and_saveexec_b64 s[18:19], vcc
	s_cbranch_execz .LBB1_8
	v_lshlrev_b32_e32 v3, 2, v0
	global_load_dword v4, v3, s[10:11]
	global_load_dword v5, v3, s[16:17]
	s_waitcnt vmcnt(0)
	ds_write2st64_b32 v3, v4, v5 offset0:136 offset1:138

.LBB1_40:
	s_or_saveexec_b64 s[8:9], s[8:9]
	v_mov_b32_e32 v9, -1
	s_xor_b64 exec, exec, s[8:9]
	s_cbranch_execz .LBB1_42
	v_lshlrev_b32_e32 v12, 2, v58
	s_waitcnt lgkmcnt(0)
	global_load_dwordx2 v[2:3], v12, s[4:5] nt
	global_load_dword v59, v12, s[4:5] offset:8 nt
	global_load_dword v5, v12, s[4:5] offset:12 nt
	global_load_dwordx4 v[6:9], v12, s[6:7] nt

.LBB1_50:
	s_or_saveexec_b64 s[8:9], s[8:9]
	v_mov_b32_e32 v17, 0
	v_mov_b32_e32 v13, -1
	s_xor_b64 exec, exec, s[8:9]
	s_cbranch_execz .LBB1_52
	v_lshlrev_b32_e32 v20, 2, v60
	s_waitcnt lgkmcnt(0)
	global_load_dwordx2 v[14:15], v20, s[4:5] nt
	global_load_dword v61, v20, s[4:5] offset:8 nt
	global_load_dword v17, v20, s[4:5] offset:12 nt
	global_load_dwordx4 v[10:13], v20, s[6:7] nt

.LBB1_60:
	s_or_saveexec_b64 s[8:9], s[8:9]
	v_mov_b32_e32 v25, 0
	v_mov_b32_e32 v21, -1
	s_xor_b64 exec, exec, s[8:9]
	s_cbranch_execz .LBB1_62
	v_lshlrev_b32_e32 v28, 2, v62
	s_waitcnt lgkmcnt(0)
	global_load_dwordx2 v[22:23], v28, s[4:5] nt
	global_load_dword v63, v28, s[4:5] offset:8 nt
	global_load_dword v25, v28, s[4:5] offset:12 nt
	global_load_dwordx4 v[18:21], v28, s[6:7] nt

.LBB1_70:
	s_or_saveexec_b64 s[8:9], s[8:9]
	v_mov_b32_e32 v33, 0
	v_mov_b32_e32 v29, -1
	s_xor_b64 exec, exec, s[8:9]
	s_cbranch_execz .LBB1_72
	v_lshlrev_b32_e32 v36, 2, v64
	s_waitcnt lgkmcnt(0)
	global_load_dwordx2 v[30:31], v36, s[4:5] nt
	global_load_dword v65, v36, s[4:5] offset:8 nt
	global_load_dword v33, v36, s[4:5] offset:12 nt
	global_load_dwordx4 v[26:29], v36, s[6:7] nt

.LBB1_80:
	s_or_saveexec_b64 s[8:9], s[8:9]
	v_mov_b32_e32 v41, 0
	v_mov_b32_e32 v37, -1
	s_xor_b64 exec, exec, s[8:9]
	s_cbranch_execz .LBB1_82
	v_lshlrev_b32_e32 v44, 2, v66
	s_waitcnt lgkmcnt(0)
	global_load_dwordx2 v[38:39], v44, s[4:5] nt
	global_load_dword v67, v44, s[4:5] offset:8 nt
	global_load_dword v41, v44, s[4:5] offset:12 nt
	global_load_dwordx4 v[34:37], v44, s[6:7] nt

.LBB1_90:
	s_or_saveexec_b64 s[8:9], s[8:9]
	v_mov_b32_e32 v49, 0
	v_mov_b32_e32 v45, -1
	s_xor_b64 exec, exec, s[8:9]
	s_cbranch_execz .LBB1_92
	v_lshlrev_b32_e32 v52, 2, v68
	s_waitcnt lgkmcnt(0)
	global_load_dwordx2 v[46:47], v52, s[4:5] nt
	global_load_dword v69, v52, s[4:5] offset:8 nt
	global_load_dword v49, v52, s[4:5] offset:12 nt
	global_load_dwordx4 v[42:45], v52, s[6:7] nt

.LBB1_100:
	s_or_saveexec_b64 s[8:9], s[8:9]
	v_mov_b32_e32 v4, 0
	v_mov_b32_e32 v53, -1
	v_mov_b32_e32 v57, 0
	s_xor_b64 exec, exec, s[8:9]
	s_cbranch_execz .LBB1_102
	v_lshlrev_b32_e32 v72, 2, v70
	s_waitcnt lgkmcnt(0)
	global_load_dwordx2 v[54:55], v72, s[4:5] nt
	global_load_dword v71, v72, s[4:5] offset:8 nt
	global_load_dword v57, v72, s[4:5] offset:12 nt
	global_load_dwordx4 v[50:53], v72, s[6:7] nt
